# P1 head-norm: xor-16/xor-32 row sums via v_permlane16/32_swap instead of serialized ds_bpermute
# speedup vs baseline: 1.0048x; 1.0041x over previous
;     __device__ __forceinline__ void operator()(Acc& acc, const Unit& u, int wr, int wc, int fr, int fq, LAS unsigned char* le, int wid, int lane, int& cpm) const {
;     ...
;                     for (int n = 0; n < 2; ++n) acc[ai][bj][m][n] = acc[ai][bj][m][n] * rs[ai][m];
;         if (!is_v) {
; #pragma unroll
;             for (int ai = 0; ai < 2; ++ai)
; #pragma unroll
;                 for (int m = 0; m < 4; ++m)
; #pragma unroll
;                     for (int bj = 0; bj < 2; ++bj) {
;                         const f32x4 a = acc[ai][bj][m][0], b = acc[ai][bj][m][1];
;                         float s = (a[0] * a[0] + a[1] * a[1]) + (a[2] * a[2] + a[3] * a[3]) + (b[0] * b[0] + b[1] * b[1]) + (b[2] * b[2] + b[3] * b[3]);
;                         s += __shfl_xor(s, 16); s += __shfl_xor(s, 32);
;                         if (fq == 0) P[((ai * 128 + wr * 64 + m * 16 + fr) * 2 + bj) * 4 + wc] = s;
.LBB0_273:
	v_pk_mul_f32 v[82:83], v[82:83], v[142:143] op_sel_hi:[1,0]
	v_pk_mul_f32 v[80:81], v[80:81], v[142:143] op_sel_hi:[1,0]
	v_pk_mul_f32 v[94:95], v[94:95], v[142:143] op_sel_hi:[1,0]
	v_pk_mul_f32 v[92:93], v[92:93], v[142:143] op_sel_hi:[1,0]
	v_pk_mul_f32 v[54:55], v[54:55], v[140:141] op_sel_hi:[1,0]
	v_pk_mul_f32 v[52:53], v[52:53], v[140:141] op_sel_hi:[1,0]
	v_pk_mul_f32 v[70:71], v[70:71], v[140:141] op_sel_hi:[1,0]
	v_pk_mul_f32 v[68:69], v[68:69], v[140:141] op_sel_hi:[1,0]
	v_pk_mul_f32 v[30:31], v[30:31], v[138:139] op_sel_hi:[1,0]
	v_pk_mul_f32 v[28:29], v[28:29], v[138:139] op_sel_hi:[1,0]
	v_pk_mul_f32 v[38:39], v[38:39], v[138:139] op_sel_hi:[1,0]
	v_pk_mul_f32 v[36:37], v[36:37], v[138:139] op_sel_hi:[1,0]
	v_pk_mul_f32 v[10:11], v[10:11], v[136:137] op_sel_hi:[1,0]
	v_pk_mul_f32 v[8:9], v[8:9], v[136:137] op_sel_hi:[1,0]
	v_pk_mul_f32 v[18:19], v[18:19], v[136:137] op_sel_hi:[1,0]
	v_pk_mul_f32 v[16:17], v[16:17], v[136:137] op_sel_hi:[1,0]
	v_pk_mul_f32 v[122:123], v[122:123], v[142:143] op_sel_hi:[1,0]
	v_pk_mul_f32 v[120:121], v[120:121], v[142:143] op_sel_hi:[1,0]
	v_pk_mul_f32 v[126:127], v[126:127], v[142:143] op_sel_hi:[1,0]
	v_pk_mul_f32 v[124:125], v[124:125], v[142:143] op_sel_hi:[1,0]
	v_pk_mul_f32 v[106:107], v[106:107], v[140:141] op_sel_hi:[1,0]
	v_pk_mul_f32 v[104:105], v[104:105], v[140:141] op_sel_hi:[1,0]
	v_pk_mul_f32 v[114:115], v[114:115], v[140:141] op_sel_hi:[1,0]
	v_pk_mul_f32 v[112:113], v[112:113], v[140:141] op_sel_hi:[1,0]
	v_pk_mul_f32 v[86:87], v[86:87], v[138:139] op_sel_hi:[1,0]
	v_pk_mul_f32 v[84:85], v[84:85], v[138:139] op_sel_hi:[1,0]
	v_pk_mul_f32 v[98:99], v[98:99], v[138:139] op_sel_hi:[1,0]
	v_pk_mul_f32 v[96:97], v[96:97], v[138:139] op_sel_hi:[1,0]
	v_pk_mul_f32 v[50:51], v[50:51], v[136:137] op_sel_hi:[1,0]
	v_pk_mul_f32 v[48:49], v[48:49], v[136:137] op_sel_hi:[1,0]
	v_pk_mul_f32 v[66:67], v[66:67], v[136:137] op_sel_hi:[1,0]
	v_pk_mul_f32 v[64:65], v[64:65], v[136:137] op_sel_hi:[1,0]
	v_pk_mul_f32 v[58:59], v[58:59], v[134:135] op_sel_hi:[1,0]
	v_pk_mul_f32 v[56:57], v[56:57], v[134:135] op_sel_hi:[1,0]
	v_pk_mul_f32 v[74:75], v[74:75], v[134:135] op_sel_hi:[1,0]
	v_pk_mul_f32 v[72:73], v[72:73], v[134:135] op_sel_hi:[1,0]
	v_pk_mul_f32 v[34:35], v[34:35], v[132:133] op_sel_hi:[1,0]
	v_pk_mul_f32 v[32:33], v[32:33], v[132:133] op_sel_hi:[1,0]
	v_pk_mul_f32 v[42:43], v[42:43], v[132:133] op_sel_hi:[1,0]
	v_pk_mul_f32 v[40:41], v[40:41], v[132:133] op_sel_hi:[1,0]
	v_pk_mul_f32 v[14:15], v[14:15], v[130:131] op_sel_hi:[1,0]
	v_pk_mul_f32 v[12:13], v[12:13], v[130:131] op_sel_hi:[1,0]
	v_pk_mul_f32 v[22:23], v[22:23], v[130:131] op_sel_hi:[1,0]
	v_pk_mul_f32 v[20:21], v[20:21], v[130:131] op_sel_hi:[1,0]
	v_pk_mul_f32 v[2:3], v[2:3], v[128:129] op_sel_hi:[1,0]
	v_pk_mul_f32 v[0:1], v[0:1], v[128:129] op_sel_hi:[1,0]
	v_pk_mul_f32 v[6:7], v[6:7], v[128:129] op_sel_hi:[1,0]
	v_pk_mul_f32 v[4:5], v[4:5], v[128:129] op_sel_hi:[1,0]
	v_pk_mul_f32 v[110:111], v[110:111], v[134:135] op_sel_hi:[1,0]
	v_pk_mul_f32 v[108:109], v[108:109], v[134:135] op_sel_hi:[1,0]
	v_pk_mul_f32 v[118:119], v[118:119], v[134:135] op_sel_hi:[1,0]
	v_pk_mul_f32 v[116:117], v[116:117], v[134:135] op_sel_hi:[1,0]
	v_pk_mul_f32 v[90:91], v[90:91], v[132:133] op_sel_hi:[1,0]
	v_pk_mul_f32 v[88:89], v[88:89], v[132:133] op_sel_hi:[1,0]
	v_pk_mul_f32 v[102:103], v[102:103], v[132:133] op_sel_hi:[1,0]
	v_pk_mul_f32 v[100:101], v[100:101], v[132:133] op_sel_hi:[1,0]
	v_pk_mul_f32 v[62:63], v[62:63], v[130:131] op_sel_hi:[1,0]
	v_pk_mul_f32 v[60:61], v[60:61], v[130:131] op_sel_hi:[1,0]
	v_pk_mul_f32 v[78:79], v[78:79], v[130:131] op_sel_hi:[1,0]
	v_pk_mul_f32 v[76:77], v[76:77], v[130:131] op_sel_hi:[1,0]
	v_pk_mul_f32 v[26:27], v[26:27], v[128:129] op_sel_hi:[1,0]
	v_pk_mul_f32 v[24:25], v[24:25], v[128:129] op_sel_hi:[1,0]
	v_pk_mul_f32 v[46:47], v[46:47], v[128:129] op_sel_hi:[1,0]
	s_andn2_b64 vcc, exec, s[14:15]
	v_pk_mul_f32 v[44:45], v[44:45], v[128:129] op_sel_hi:[1,0]
	s_cbranch_vccnz .LBB0_378
	v_mul_f32_e32 v128, v81, v81
	v_mul_f32_e32 v129, v83, v83
	v_fmac_f32_e32 v128, v80, v80
	v_fmac_f32_e32 v129, v82, v82
	v_add_f32_e32 v128, v128, v129
	v_mul_f32_e32 v129, v93, v93
	v_fmac_f32_e32 v129, v92, v92
	v_add_f32_e32 v128, v129, v128
	v_mul_f32_e32 v129, v95, v95
	v_fmac_f32_e32 v129, v94, v94
	v_add_f32_e32 v128, v129, v128
	v_mov_b32_e32 v129, v128
	s_nop 1
	v_permlane16_swap_b32_e32 v129, v128
	s_waitcnt lgkmcnt(0)
	v_add_f32_e32 v129, v128, v129
	v_mov_b32_e32 v130, v129
	s_nop 1
	v_permlane32_swap_b32_e32 v130, v129
	v_add_u32_e32 v128, s62, v199
	s_and_saveexec_b64 s[14:15], s[8:9]
	s_cbranch_execz .LBB0_276
	s_waitcnt lgkmcnt(0)
	v_add_f32_e32 v129, v129, v130
	ds_write_b32 v128, v129
.LBB0_276:
	s_or_b64 exec, exec, s[14:15]
	v_mul_f32_e32 v129, v121, v121
	s_waitcnt lgkmcnt(0)
	v_mul_f32_e32 v130, v123, v123
	v_fmac_f32_e32 v129, v120, v120
	v_fmac_f32_e32 v130, v122, v122
	v_add_f32_e32 v129, v129, v130
	v_mul_f32_e32 v130, v125, v125
	v_fmac_f32_e32 v130, v124, v124
	v_add_f32_e32 v129, v130, v129
	v_mul_f32_e32 v130, v127, v127
	v_fmac_f32_e32 v130, v126, v126
	v_add_f32_e32 v129, v130, v129
	v_mov_b32_e32 v130, v129
	s_nop 1
	v_permlane16_swap_b32_e32 v130, v129
	s_waitcnt lgkmcnt(0)
	v_add_f32_e32 v129, v129, v130
	v_mov_b32_e32 v130, v129
	s_nop 1
	v_permlane32_swap_b32_e32 v130, v129
	s_and_saveexec_b64 s[14:15], s[8:9]
	s_cbranch_execz .LBB0_278
	s_waitcnt lgkmcnt(0)
	v_add_f32_e32 v129, v129, v130
	ds_write_b32 v128, v129 offset:16
;     __device__ __forceinline__ void operator()(Acc& acc, const Unit& u, int wr, int wc, int fr, int fq, LAS unsigned char* le, int wid, int lane, int& cpm) const {
;     ...
;             for (int ai = 0; ai < 2; ++ai)
; #pragma unroll
;                 for (int m = 0; m < 4; ++m)
; #pragma unroll
;                     for (int bj = 0; bj < 2; ++bj) {
;                         const f32x4 a = acc[ai][bj][m][0], b = acc[ai][bj][m][1];
;                         float s = (a[0] * a[0] + a[1] * a[1]) + (a[2] * a[2] + a[3] * a[3]) + (b[0] * b[0] + b[1] * b[1]) + (b[2] * b[2] + b[3] * b[3]);
;                         s += __shfl_xor(s, 16); s += __shfl_xor(s, 32);
;                         if (fq == 0) P[((ai * 128 + wr * 64 + m * 16 + fr) * 2 + bj) * 4 + wc] = s;
.LBB0_278:
	s_or_b64 exec, exec, s[14:15]
	v_mul_f32_e32 v129, v53, v53
	s_waitcnt lgkmcnt(0)
	v_mul_f32_e32 v130, v55, v55
	v_fmac_f32_e32 v129, v52, v52
	v_fmac_f32_e32 v130, v54, v54
	v_add_f32_e32 v129, v129, v130
	v_mul_f32_e32 v130, v69, v69
	v_fmac_f32_e32 v130, v68, v68
	v_add_f32_e32 v129, v130, v129
	v_mul_f32_e32 v130, v71, v71
	v_fmac_f32_e32 v130, v70, v70
	v_add_f32_e32 v129, v130, v129
	v_mov_b32_e32 v130, v129
	s_nop 1
	v_permlane16_swap_b32_e32 v130, v129
	s_waitcnt lgkmcnt(0)
	v_add_f32_e32 v129, v129, v130
	v_mov_b32_e32 v130, v129
	s_nop 1
	v_permlane32_swap_b32_e32 v130, v129
	s_and_saveexec_b64 s[14:15], s[8:9]
	s_cbranch_execz .LBB0_280
	s_waitcnt lgkmcnt(0)
	v_add_f32_e32 v129, v129, v130
	ds_write_b32 v128, v129 offset:512
.LBB0_280:
	s_or_b64 exec, exec, s[14:15]
	v_mul_f32_e32 v129, v105, v105
	s_waitcnt lgkmcnt(0)
	v_mul_f32_e32 v130, v107, v107
	v_fmac_f32_e32 v129, v104, v104
	v_fmac_f32_e32 v130, v106, v106
	v_add_f32_e32 v129, v129, v130
	v_mul_f32_e32 v130, v113, v113
	v_fmac_f32_e32 v130, v112, v112
	v_add_f32_e32 v129, v130, v129
	v_mul_f32_e32 v130, v115, v115
	v_fmac_f32_e32 v130, v114, v114
	v_add_f32_e32 v129, v130, v129
	v_mov_b32_e32 v130, v129
	s_nop 1
	v_permlane16_swap_b32_e32 v130, v129
	s_waitcnt lgkmcnt(0)
	v_add_f32_e32 v129, v129, v130
	v_mov_b32_e32 v130, v129
	s_nop 1
	v_permlane32_swap_b32_e32 v130, v129
	s_and_saveexec_b64 s[14:15], s[8:9]
	s_cbranch_execz .LBB0_282
	s_waitcnt lgkmcnt(0)
	v_add_f32_e32 v129, v129, v130
	ds_write_b32 v128, v129 offset:528
.LBB0_282:
	s_or_b64 exec, exec, s[14:15]
	v_mul_f32_e32 v129, v29, v29
	s_waitcnt lgkmcnt(0)
	v_mul_f32_e32 v130, v31, v31
	v_fmac_f32_e32 v129, v28, v28
	v_fmac_f32_e32 v130, v30, v30
	v_add_f32_e32 v129, v129, v130
	v_mul_f32_e32 v130, v37, v37
	v_fmac_f32_e32 v130, v36, v36
	v_add_f32_e32 v129, v130, v129
	v_mul_f32_e32 v130, v39, v39
	v_fmac_f32_e32 v130, v38, v38
	v_add_f32_e32 v129, v130, v129
	v_mov_b32_e32 v130, v129
	s_nop 1
	v_permlane16_swap_b32_e32 v130, v129
	s_waitcnt lgkmcnt(0)
	v_add_f32_e32 v129, v129, v130
	v_mov_b32_e32 v130, v129
	s_nop 1
	v_permlane32_swap_b32_e32 v130, v129
	s_and_saveexec_b64 s[14:15], s[8:9]
	s_cbranch_execz .LBB0_284
	s_waitcnt lgkmcnt(0)
	v_add_f32_e32 v129, v129, v130
	ds_write_b32 v128, v129 offset:1024
.LBB0_284:
	s_or_b64 exec, exec, s[14:15]
	v_mul_f32_e32 v129, v85, v85
	s_waitcnt lgkmcnt(0)
	v_mul_f32_e32 v130, v87, v87
	v_fmac_f32_e32 v129, v84, v84
	v_fmac_f32_e32 v130, v86, v86
	v_add_f32_e32 v129, v129, v130
	v_mul_f32_e32 v130, v97, v97
	v_fmac_f32_e32 v130, v96, v96
	v_add_f32_e32 v129, v130, v129
	v_mul_f32_e32 v130, v99, v99
	v_fmac_f32_e32 v130, v98, v98
	v_add_f32_e32 v129, v130, v129
	v_mov_b32_e32 v130, v129
	s_nop 1
	v_permlane16_swap_b32_e32 v130, v129
	s_waitcnt lgkmcnt(0)
	v_add_f32_e32 v129, v129, v130
	v_mov_b32_e32 v130, v129
	s_nop 1
	v_permlane32_swap_b32_e32 v130, v129
	s_and_saveexec_b64 s[14:15], s[8:9]
	s_cbranch_execz .LBB0_286
	s_waitcnt lgkmcnt(0)
	v_add_f32_e32 v129, v129, v130
	ds_write_b32 v128, v129 offset:1040
.LBB0_286:
	s_or_b64 exec, exec, s[14:15]
	v_mul_f32_e32 v129, v9, v9
	s_waitcnt lgkmcnt(0)
	v_mul_f32_e32 v130, v11, v11
	v_fmac_f32_e32 v129, v8, v8
	v_fmac_f32_e32 v130, v10, v10
	v_add_f32_e32 v129, v129, v130
	v_mul_f32_e32 v130, v17, v17
	v_fmac_f32_e32 v130, v16, v16
	v_add_f32_e32 v129, v130, v129
	v_mul_f32_e32 v130, v19, v19
	v_fmac_f32_e32 v130, v18, v18
	v_add_f32_e32 v129, v130, v129
	v_mov_b32_e32 v130, v129
	s_nop 1
	v_permlane16_swap_b32_e32 v130, v129
	s_waitcnt lgkmcnt(0)
	v_add_f32_e32 v129, v129, v130
	v_mov_b32_e32 v130, v129
	s_nop 1
	v_permlane32_swap_b32_e32 v130, v129
	s_and_saveexec_b64 s[14:15], s[8:9]
	s_cbranch_execz .LBB0_288
	s_waitcnt lgkmcnt(0)
	v_add_f32_e32 v129, v129, v130
	ds_write_b32 v128, v129 offset:1536
.LBB0_288:
	s_or_b64 exec, exec, s[14:15]
	v_mul_f32_e32 v129, v49, v49
	s_waitcnt lgkmcnt(0)
	v_mul_f32_e32 v130, v51, v51
	v_fmac_f32_e32 v129, v48, v48
	v_fmac_f32_e32 v130, v50, v50
	v_add_f32_e32 v129, v129, v130
	v_mul_f32_e32 v130, v65, v65
	v_fmac_f32_e32 v130, v64, v64
	v_add_f32_e32 v129, v130, v129
	v_mul_f32_e32 v130, v67, v67
	v_fmac_f32_e32 v130, v66, v66
	v_add_f32_e32 v129, v130, v129
	v_mov_b32_e32 v130, v129
	s_nop 1
	v_permlane16_swap_b32_e32 v130, v129
	s_waitcnt lgkmcnt(0)
	v_add_f32_e32 v129, v129, v130
	v_mov_b32_e32 v130, v129
	s_nop 1
	v_permlane32_swap_b32_e32 v130, v129
	s_and_saveexec_b64 s[14:15], s[8:9]
	s_cbranch_execz .LBB0_290
	s_waitcnt lgkmcnt(0)
	v_add_f32_e32 v129, v129, v130
	ds_write_b32 v128, v129 offset:1552
.LBB0_290:
	s_or_b64 exec, exec, s[14:15]
	v_mul_f32_e32 v129, v57, v57
	s_waitcnt lgkmcnt(0)
	v_mul_f32_e32 v130, v59, v59
	v_fmac_f32_e32 v129, v56, v56
	v_fmac_f32_e32 v130, v58, v58
	v_add_f32_e32 v129, v129, v130
	v_mul_f32_e32 v130, v73, v73
	v_fmac_f32_e32 v130, v72, v72
	v_add_f32_e32 v129, v130, v129
	v_mul_f32_e32 v130, v75, v75
	v_fmac_f32_e32 v130, v74, v74
	v_add_f32_e32 v129, v130, v129
	v_mov_b32_e32 v130, v129
	s_nop 1
	v_permlane16_swap_b32_e32 v130, v129
	s_waitcnt lgkmcnt(0)
	v_add_f32_e32 v129, v129, v130
	v_mov_b32_e32 v130, v129
	s_nop 1
	v_permlane32_swap_b32_e32 v130, v129
	s_and_saveexec_b64 s[14:15], s[8:9]
	s_cbranch_execz .LBB0_292
	s_waitcnt lgkmcnt(0)
	v_add_f32_e32 v129, v129, v130
	ds_write_b32 v128, v129 offset:4096
;     __device__ __forceinline__ void operator()(Acc& acc, const Unit& u, int wr, int wc, int fr, int fq, LAS unsigned char* le, int wid, int lane, int& cpm) const {
;     ...
;             for (int ai = 0; ai < 2; ++ai)
; #pragma unroll
;                 for (int m = 0; m < 4; ++m)
; #pragma unroll
;                     for (int bj = 0; bj < 2; ++bj) {
;                         const f32x4 a = acc[ai][bj][m][0], b = acc[ai][bj][m][1];
;                         float s = (a[0] * a[0] + a[1] * a[1]) + (a[2] * a[2] + a[3] * a[3]) + (b[0] * b[0] + b[1] * b[1]) + (b[2] * b[2] + b[3] * b[3]);
;                         s += __shfl_xor(s, 16); s += __shfl_xor(s, 32);
;                         if (fq == 0) P[((ai * 128 + wr * 64 + m * 16 + fr) * 2 + bj) * 4 + wc] = s;
.LBB0_292:
	s_or_b64 exec, exec, s[14:15]
	v_mul_f32_e32 v129, v109, v109
	s_waitcnt lgkmcnt(0)
	v_mul_f32_e32 v130, v111, v111
	v_fmac_f32_e32 v129, v108, v108
	v_fmac_f32_e32 v130, v110, v110
	v_add_f32_e32 v129, v129, v130
	v_mul_f32_e32 v130, v117, v117
	v_fmac_f32_e32 v130, v116, v116
	v_add_f32_e32 v129, v130, v129
	v_mul_f32_e32 v130, v119, v119
	v_fmac_f32_e32 v130, v118, v118
	v_add_f32_e32 v129, v130, v129
	v_mov_b32_e32 v130, v129
	s_nop 1
	v_permlane16_swap_b32_e32 v130, v129
	s_waitcnt lgkmcnt(0)
	v_add_f32_e32 v129, v129, v130
	v_mov_b32_e32 v130, v129
	s_nop 1
	v_permlane32_swap_b32_e32 v130, v129
	s_and_saveexec_b64 s[14:15], s[8:9]
	s_cbranch_execz .LBB0_294
	s_waitcnt lgkmcnt(0)
	v_add_f32_e32 v129, v129, v130
	ds_write_b32 v128, v129 offset:4112
.LBB0_294:
	s_or_b64 exec, exec, s[14:15]
	v_mul_f32_e32 v129, v33, v33
	s_waitcnt lgkmcnt(0)
	v_mul_f32_e32 v130, v35, v35
	v_fmac_f32_e32 v129, v32, v32
	v_fmac_f32_e32 v130, v34, v34
	v_add_f32_e32 v129, v129, v130
	v_mul_f32_e32 v130, v41, v41
	v_fmac_f32_e32 v130, v40, v40
	v_add_f32_e32 v129, v130, v129
	v_mul_f32_e32 v130, v43, v43
	v_fmac_f32_e32 v130, v42, v42
	v_add_f32_e32 v129, v130, v129
	v_mov_b32_e32 v130, v129
	s_nop 1
	v_permlane16_swap_b32_e32 v130, v129
	s_waitcnt lgkmcnt(0)
	v_add_f32_e32 v129, v129, v130
	v_mov_b32_e32 v130, v129
	s_nop 1
	v_permlane32_swap_b32_e32 v130, v129
	s_and_saveexec_b64 s[14:15], s[8:9]
	s_cbranch_execz .LBB0_296
	s_waitcnt lgkmcnt(0)
	v_add_f32_e32 v129, v129, v130
	ds_write_b32 v128, v129 offset:4608
.LBB0_296:
	s_or_b64 exec, exec, s[14:15]
	v_mul_f32_e32 v129, v89, v89
	s_waitcnt lgkmcnt(0)
	v_mul_f32_e32 v130, v91, v91
	v_fmac_f32_e32 v129, v88, v88
	v_fmac_f32_e32 v130, v90, v90
	v_add_f32_e32 v129, v129, v130
	v_mul_f32_e32 v130, v101, v101
	v_fmac_f32_e32 v130, v100, v100
	v_add_f32_e32 v129, v130, v129
	v_mul_f32_e32 v130, v103, v103
	v_fmac_f32_e32 v130, v102, v102
	v_add_f32_e32 v129, v130, v129
	v_mov_b32_e32 v130, v129
	s_nop 1
	v_permlane16_swap_b32_e32 v130, v129
	s_waitcnt lgkmcnt(0)
	v_add_f32_e32 v129, v129, v130
	v_mov_b32_e32 v130, v129
	s_nop 1
	v_permlane32_swap_b32_e32 v130, v129
	s_and_saveexec_b64 s[14:15], s[8:9]
	s_cbranch_execz .LBB0_298
	s_waitcnt lgkmcnt(0)
	v_add_f32_e32 v129, v129, v130
	ds_write_b32 v128, v129 offset:4624
.LBB0_298:
	s_or_b64 exec, exec, s[14:15]
	v_mul_f32_e32 v129, v13, v13
	s_waitcnt lgkmcnt(0)
	v_mul_f32_e32 v130, v15, v15
	v_fmac_f32_e32 v129, v12, v12
	v_fmac_f32_e32 v130, v14, v14
	v_add_f32_e32 v129, v129, v130
	v_mul_f32_e32 v130, v21, v21
	v_fmac_f32_e32 v130, v20, v20
	v_add_f32_e32 v129, v130, v129
	v_mul_f32_e32 v130, v23, v23
	v_fmac_f32_e32 v130, v22, v22
	v_add_f32_e32 v129, v130, v129
	v_mov_b32_e32 v130, v129
	s_nop 1
	v_permlane16_swap_b32_e32 v130, v129
	s_waitcnt lgkmcnt(0)
	v_add_f32_e32 v129, v129, v130
	v_mov_b32_e32 v130, v129
	s_nop 1
	v_permlane32_swap_b32_e32 v130, v129
	s_and_saveexec_b64 s[14:15], s[8:9]
	s_cbranch_execz .LBB0_300
	s_waitcnt lgkmcnt(0)
	v_add_f32_e32 v129, v129, v130
	ds_write_b32 v128, v129 offset:5120
.LBB0_300:
	s_or_b64 exec, exec, s[14:15]
	v_mul_f32_e32 v129, v61, v61
	s_waitcnt lgkmcnt(0)
	v_mul_f32_e32 v130, v63, v63
	v_fmac_f32_e32 v129, v60, v60
	v_fmac_f32_e32 v130, v62, v62
	v_add_f32_e32 v129, v129, v130
	v_mul_f32_e32 v130, v77, v77
	v_fmac_f32_e32 v130, v76, v76
	v_add_f32_e32 v129, v130, v129
	v_mul_f32_e32 v130, v79, v79
	v_fmac_f32_e32 v130, v78, v78
	v_add_f32_e32 v129, v130, v129
	v_mov_b32_e32 v130, v129
	s_nop 1
	v_permlane16_swap_b32_e32 v130, v129
	s_waitcnt lgkmcnt(0)
	v_add_f32_e32 v129, v129, v130
	v_mov_b32_e32 v130, v129
	s_nop 1
	v_permlane32_swap_b32_e32 v130, v129
	s_and_saveexec_b64 s[14:15], s[8:9]
	s_cbranch_execz .LBB0_302
	s_waitcnt lgkmcnt(0)
	v_add_f32_e32 v129, v129, v130
	ds_write_b32 v128, v129 offset:5136
.LBB0_302:
	s_or_b64 exec, exec, s[14:15]
	v_mul_f32_e32 v129, v1, v1
	s_waitcnt lgkmcnt(0)
	v_mul_f32_e32 v130, v3, v3
	v_fmac_f32_e32 v129, v0, v0
	v_fmac_f32_e32 v130, v2, v2
	v_add_f32_e32 v129, v129, v130
	v_mul_f32_e32 v130, v5, v5
	v_fmac_f32_e32 v130, v4, v4
	v_add_f32_e32 v129, v130, v129
	v_mul_f32_e32 v130, v7, v7
	v_fmac_f32_e32 v130, v6, v6
	v_add_f32_e32 v129, v130, v129
	v_mov_b32_e32 v130, v129
	s_nop 1
	v_permlane16_swap_b32_e32 v130, v129
	s_waitcnt lgkmcnt(0)
	v_add_f32_e32 v129, v129, v130
	v_mov_b32_e32 v130, v129
	s_nop 1
	v_permlane32_swap_b32_e32 v130, v129
	s_and_saveexec_b64 s[14:15], s[8:9]
	s_cbranch_execz .LBB0_304
	s_waitcnt lgkmcnt(0)
	v_add_f32_e32 v129, v129, v130
	ds_write_b32 v128, v129 offset:5632
.LBB0_304:
	s_or_b64 exec, exec, s[14:15]
	v_mul_f32_e32 v129, v25, v25
	s_waitcnt lgkmcnt(0)
	v_mul_f32_e32 v130, v27, v27
	v_fmac_f32_e32 v129, v24, v24
	v_fmac_f32_e32 v130, v26, v26
	v_add_f32_e32 v129, v129, v130
	v_mul_f32_e32 v130, v45, v45
	v_fmac_f32_e32 v130, v44, v44
	v_add_f32_e32 v129, v130, v129
	v_mul_f32_e32 v130, v47, v47
	v_fmac_f32_e32 v130, v46, v46
	v_add_f32_e32 v129, v130, v129
	v_mov_b32_e32 v130, v129
	s_nop 1
	v_permlane16_swap_b32_e32 v130, v129
	s_waitcnt lgkmcnt(0)
	v_add_f32_e32 v129, v129, v130
	v_mov_b32_e32 v130, v129
	s_nop 1
	v_permlane32_swap_b32_e32 v130, v129
	s_and_saveexec_b64 s[14:15], s[8:9]
	s_cbranch_execz .LBB0_306
	s_waitcnt lgkmcnt(0)
	v_add_f32_e32 v129, v129, v130
	ds_write_b32 v128, v129 offset:5648
